# attention: tile T+2 LDS-DMA issued after the 4th QK MFMA instead of right after the tile barrier
# baseline (speedup 1.0000x reference)
; #define LAS __attribute__((address_space(3)))
; __device__ __forceinline__ float half_swap_max(float m) { unsigned a = __builtin_bit_cast(unsigned, m), b = a; half_swap(a, b); return __builtin_fmaxf(__builtin_bit_cast(float, a), __builtin_bit_cast(float, b)); }
; #define EX2(P, i) do { P[i] = __builtin_amdgcn_exp2f(P[i]); P[(i) + 1] = __builtin_amdgcn_exp2f(P[(i) + 1]); } while (0)
; #define PK8(P, i) ({ v4u w_; w_.x = pk2(P[i], P[(i) + 1]); w_.y = pk2(P[(i) + 2], P[(i) + 3]); w_.z = pk2(P[(i) + 4], P[(i) + 5]); w_.w = pk2(P[(i) + 6], P[(i) + 7]); __builtin_bit_cast(bf16x8, w_); })
; __device__ __forceinline__ void attn_unit(LAS unsigned char* lds, const bf16* proj, bf16* Y, const float* relb, const float* hgain, float lam, float oscale, int b, int h, int qb, int tid, int lane, int wid, Stopwatch& sw) {
;     ...
;       float mt = __builtin_fmaxf(sA0[0], sA1[0]);
; #pragma unroll
;       for (int r = 1; r < 16; ++r) mt = __builtin_fmaxf(mt, __builtin_fmaxf(sA0[r], sA1[r]));
;       mt = half_swap_max(mt); m_run = mt;
; #pragma unroll
;       for (int r = 0; r < 16; ++r) { sA0[r] -= mt; sA1[r] -= mt; } }
;     int sc = 0, sn = 32768, sn2 = 65536;
;     ...
;     bf16x8 qreg[4];
; #pragma unroll
;     for (int d0 = 0; d0 < 4; ++d0) qreg[d0] = *(const LAS bf16x8*)(qlds + d0 * 1024);
;     bf16x8 pw0, pw1, pw2, pw3;
;     {
; #pragma unroll
;       for (int r = 0; r < 16; r += 2) { EX2(sA0, r); EX2(sA1, r); }
;       float sm_ = 0.f;
; #pragma unroll
;       for (int r = 0; r < 16; ++r) sm_ += sA0[r] + sA1[r];
;       l_run += sm_; pw0 = PK8(sA0, 0); pw1 = PK8(sA0, 8); pw2 = PK8(sA1, 0); pw3 = PK8(sA1, 8); }
.LBB0_394:
	v_and_b32_e32 v166, 63, v61
	v_lshrrev_b32_e32 v36, 2, v61
	v_lshlrev_b32_e32 v41, 3, v166
	v_and_b32_e32 v36, 11, v36
	v_lshrrev_b32_e32 v37, 3, v61
	v_and_b32_e32 v38, 1, v63
	v_and_b32_e32 v41, 8, v41
	v_and_or_b32 v37, v37, 2, v38
	v_lshrrev_b32_e32 v39, 2, v36
	v_lshl_or_b32 v42, v36, 8, v41
	v_or_b32_e32 v36, 4, v36
	v_and_b32_e32 v38, 12, v61
	v_lshrrev_b32_e32 v43, 2, v36
	v_lshl_or_b32 v41, v36, 8, v41
	v_or_b32_e32 v36, 4, v37
	v_bitop3_b32 v46, v43, v36, v38 bitop3:0x36
	v_or_b32_e32 v36, 8, v37
	v_or_b32_e32 v40, v39, v38
	v_bitop3_b32 v48, v43, v36, v38 bitop3:0x36
	v_or_b32_e32 v36, 12, v37
	v_bitop3_b32 v39, v39, v37, v38 bitop3:0x36
	v_bitop3_b32 v44, v43, v37, v38 bitop3:0x36
	v_bitop3_b32 v45, v37, v40, 4 bitop3:0x36
	v_bitop3_b32 v47, v37, v40, 8 bitop3:0x36
	v_bitop3_b32 v40, v37, v40, 12 bitop3:0x36
	v_bitop3_b32 v38, v43, v36, v38 bitop3:0x36
	v_max_f32_e32 v36, v5, v5
	v_max_f32_e32 v37, v21, v21
	v_max_f32_e32 v36, v37, v36
	v_max_f32_e32 v37, v6, v6
	v_max_f32_e32 v43, v22, v22
	v_max_f32_e32 v37, v43, v37
	v_max_f32_e32 v43, v7, v7
	v_max_f32_e32 v49, v23, v23
	v_max3_f32 v36, v20, v4, v36
	v_max_f32_e32 v43, v49, v43
	v_max3_f32 v36, v36, v37, v43
	v_max_f32_e32 v37, v8, v8
	v_max_f32_e32 v43, v24, v24
	v_max_f32_e32 v37, v43, v37
	v_max_f32_e32 v43, v9, v9
	v_max_f32_e32 v49, v25, v25
	v_max_f32_e32 v43, v49, v43
	v_max3_f32 v36, v36, v37, v43
	v_max_f32_e32 v37, v10, v10
	v_max_f32_e32 v43, v26, v26
	v_max_f32_e32 v37, v43, v37
	v_max_f32_e32 v43, v11, v11
	v_max_f32_e32 v49, v27, v27
	v_max_f32_e32 v43, v49, v43
	v_max3_f32 v36, v36, v37, v43
	v_max_f32_e32 v37, v12, v12
	v_max_f32_e32 v43, v28, v28
	v_max_f32_e32 v37, v43, v37
	v_max_f32_e32 v43, v13, v13
	v_max_f32_e32 v49, v29, v29
	v_max_f32_e32 v43, v49, v43
	v_max3_f32 v36, v36, v37, v43
	v_max_f32_e32 v37, v14, v14
	v_max_f32_e32 v43, v30, v30
	v_max_f32_e32 v37, v43, v37
	v_max_f32_e32 v43, v15, v15
	v_max_f32_e32 v49, v31, v31
	v_max_f32_e32 v43, v49, v43
	v_max3_f32 v36, v36, v37, v43
	v_max_f32_e32 v37, v16, v16
	v_max_f32_e32 v43, v32, v32
	v_max_f32_e32 v37, v43, v37
	v_max_f32_e32 v43, v17, v17
	v_max_f32_e32 v49, v33, v33
	v_max_f32_e32 v43, v49, v43
	v_max3_f32 v36, v36, v37, v43
	v_max_f32_e32 v37, v18, v18
	v_max_f32_e32 v43, v34, v34
	v_max_f32_e32 v37, v43, v37
	v_max_f32_e32 v43, v19, v19
	v_max_f32_e32 v49, v35, v35
	v_max_f32_e32 v43, v49, v43
	v_max3_f32 v36, v36, v37, v43
	v_mov_b32_e32 v37, v36
	s_nop 1
	v_permlane32_swap_b32 v36, v37
	s_nop 1
	ds_read_b128 v[116:119], v62
	ds_read_b128 v[120:123], v62 offset:1024
	ds_read_b128 v[124:127], v62 offset:2048
	ds_read_b128 v[128:131], v62 offset:3072
	v_max_f32_e32 v37, v37, v37
	v_max_f32_e32 v36, v36, v36
	v_max_f32_e32 v167, v36, v37
	v_sub_f32_e32 v20, v20, v167
	v_sub_f32_e32 v36, v4, v167
	v_sub_f32_e32 v4, v21, v167
	v_sub_f32_e32 v5, v5, v167
	v_exp_f32_e32 v62, v20
	v_exp_f32_e32 v63, v36
	v_sub_f32_e32 v21, v22, v167
	v_sub_f32_e32 v22, v6, v167
	v_exp_f32_e32 v4, v4
	v_exp_f32_e32 v6, v5
	v_sub_f32_e32 v23, v23, v167
	v_sub_f32_e32 v7, v7, v167
	v_exp_f32_e32 v64, v21
	v_exp_f32_e32 v65, v22
	v_sub_f32_e32 v37, v8, v167
	v_sub_f32_e32 v43, v10, v167
	v_exp_f32_e32 v8, v23
	v_exp_f32_e32 v10, v7
	v_add_f32_e32 v5, v62, v63
	v_mov_b32_e32 v7, v3
	v_sub_f32_e32 v24, v24, v167
	v_exp_f32_e32 v67, v37
	v_pk_add_f32 v[36:37], v[4:5], v[6:7]
	v_sub_f32_e32 v25, v25, v167
	v_sub_f32_e32 v9, v9, v167
	v_sub_f32_e32 v11, v11, v167
	v_exp_f32_e32 v66, v24
	v_pk_add_f32 v[36:37], v[36:37], v[36:37] op_sel_hi:[0,1]
	v_sub_f32_e32 v49, v12, v167
	v_sub_f32_e32 v50, v14, v167
	v_sub_f32_e32 v61, v18, v167
	v_exp_f32_e32 v12, v25
	v_exp_f32_e32 v14, v9
	v_exp_f32_e32 v18, v11
	v_add_f32_e32 v9, v64, v65
	v_mov_b32_e32 v11, v37
	v_sub_f32_e32 v26, v26, v167
	v_pk_add_f32 v[36:37], v[8:9], v[10:11]
	v_sub_f32_e32 v27, v27, v167
	v_sub_f32_e32 v13, v13, v167
	v_sub_f32_e32 v15, v15, v167
	v_exp_f32_e32 v68, v26
	v_exp_f32_e32 v43, v43
	v_pk_add_f32 v[36:37], v[36:37], v[36:37] op_sel_hi:[0,1]
	v_sub_f32_e32 v51, v16, v167
	v_exp_f32_e32 v16, v27
	v_exp_f32_e32 v22, v13
	v_exp_f32_e32 v26, v15
	v_add_f32_e32 v13, v66, v67
	v_mov_b32_e32 v15, v37
	v_sub_f32_e32 v28, v28, v167
	v_pk_add_f32 v[36:37], v[12:13], v[14:15]
	v_sub_f32_e32 v29, v29, v167
	v_sub_f32_e32 v30, v30, v167
	v_sub_f32_e32 v17, v17, v167
	v_sub_f32_e32 v34, v34, v167
	v_sub_f32_e32 v19, v19, v167
	v_exp_f32_e32 v69, v28
	v_exp_f32_e32 v49, v49
	v_pk_add_f32 v[36:37], v[36:37], v[36:37] op_sel_hi:[0,1]
	v_exp_f32_e32 v20, v29
	v_exp_f32_e32 v70, v30
	v_exp_f32_e32 v30, v17
	v_exp_f32_e32 v72, v34
	v_exp_f32_e32 v34, v19
	v_add_f32_e32 v17, v68, v43
	v_mov_b32_e32 v19, v37
	v_pk_add_f32 v[36:37], v[16:17], v[18:19]
	v_sub_f32_e32 v31, v31, v167
	v_exp_f32_e32 v50, v50
	v_pk_add_f32 v[36:37], v[36:37], v[36:37] op_sel_hi:[0,1]
	v_exp_f32_e32 v24, v31
	v_add_f32_e32 v21, v69, v49
	v_mov_b32_e32 v23, v37
	v_sub_f32_e32 v32, v32, v167
	v_pk_add_f32 v[36:37], v[20:21], v[22:23]
	v_sub_f32_e32 v33, v33, v167
	v_exp_f32_e32 v71, v32
	v_exp_f32_e32 v51, v51
	v_pk_add_f32 v[36:37], v[36:37], v[36:37] op_sel_hi:[0,1]
	v_exp_f32_e32 v28, v33
	v_add_f32_e32 v25, v70, v50
	v_mov_b32_e32 v27, v37
	v_pk_add_f32 v[36:37], v[24:25], v[26:27]
	v_sub_f32_e32 v35, v35, v167
	v_exp_f32_e32 v61, v61
	v_pk_add_f32 v[36:37], v[36:37], v[36:37] op_sel_hi:[0,1]
	v_exp_f32_e32 v32, v35
	v_add_f32_e32 v29, v71, v51
	v_mov_b32_e32 v31, v37
	v_pk_add_f32 v[36:37], v[28:29], v[30:31]
	v_add_f32_e32 v33, v72, v61
	v_pk_add_f32 v[36:37], v[36:37], v[36:37] op_sel_hi:[0,1]
	v_mov_b32_e32 v35, v37
	s_lshl_b32 s18, s0, 7
	v_pk_add_f32 v[36:37], v[32:33], v[34:35]
; #define TS_END(sw, id) do { if ((id) == TSSEL && (sw).on) (sw).acc += __builtin_amdgcn_s_memrealtime() - (sw).t0; } while (0)
; #define TS_END(sw, id) do { } while (0)
; #define LAS __attribute__((address_space(3)))
; __device__ __forceinline__ void attn_unit(LAS unsigned char* lds, const bf16* proj, bf16* Y, const float* relb, const float* hgain, float lam, float oscale, int b, int h, int qb, int tid, int lane, int wid, Stopwatch& sw) {
;     ...
;     unsigned va[4][2];
; #pragma unroll
;     for (int c = 0; c < 4; ++c) { va[c][0] = 16384u + tr_off(lane, c, 0); va[c][1] = 16384u + tr_off(lane, c, 1); }
;     const unsigned kboff = mp * 8192 + hi * 1024 + r32 * 16;
;     const int NT = 2 * qb + 2;
;     ATT_DMA(0, lds); ATT_DMA(1, lds + 32768);
;     float m_run = -1e30f, l_run = 0.f;
;     f32x16 o[4];
; #pragma unroll
;     for (int c = 0; c < 4; ++c) o[c] = splat16(0.f);
;     const int qi = qw + r32;
;     ...
;     WG_BAR();
;     TS_END(sw, 8);
;     f32x16 sA0, sA1, sB0, sB1;
;     typedef __bf16 bf2_t_ __attribute__((ext_vector_type(2)));
;     const bf2_t_ one2 = __builtin_bit_cast(bf2_t_, 0x3F803F80u);
;     { const bool far0 = (63 + 128 <= qw); ATT_QK(sA0, sA1, lds, far0 ? bias31 : 0.f);
;       if (!far0) {
; #pragma unroll
;           for (int r = 0; r < 16; ++r) { const int key = 16 * (r >> 3) + 8 * hi + (r & 7); const int d0_ = qi - key, d1_ = d0_ - 32;
;               const float b0 = tab[d0_ < 0 ? 0 : (d0_ > 128 ? 128 : d0_)], b1 = tab[d1_ < 0 ? 0 : (d1_ > 128 ? 128 : d1_)];
;               sA0[r] = d0_ < 0 ? -1e30f : sA0[r] + b0; sA1[r] = d1_ < 0 ? -1e30f : sA1[r] + b1; } }
;       float mt = __builtin_fmaxf(sA0[0], sA1[0]);
; #pragma unroll
;       for (int r = 1; r < 16; ++r) mt = __builtin_fmaxf(mt, __builtin_fmaxf(sA0[r], sA1[r]));
;       mt = half_swap_max(mt); m_run = mt;
; #pragma unroll
;       for (int r = 0; r < 16; ++r) { sA0[r] -= mt; sA1[r] -= mt; } }
;     int sc = 0, sn = 32768, sn2 = 65536;
;     ...
;     bf16x8 qreg[4];
; #pragma unroll
;     for (int d0 = 0; d0 < 4; ++d0) qreg[d0] = *(const LAS bf16x8*)(qlds + d0 * 1024);
;     bf16x8 pw0, pw1, pw2, pw3;
;     {
; #pragma unroll
;       for (int r = 0; r < 16; r += 2) { EX2(sA0, r); EX2(sA1, r); }
;       float sm_ = 0.f;
; #pragma unroll
;       for (int r = 0; r < 16; ++r) sm_ += sA0[r] + sA1[r];
;       l_run += sm_; pw0 = PK8(sA0, 0); pw1 = PK8(sA0, 8); pw2 = PK8(sA1, 0); pw3 = PK8(sA1, 8); }
	s_mov_b64 s[36:37], 0x380000
	v_readlane_b32 s0, v252, 60
	v_add_f32_e32 v5, v36, v37
	v_cvt_pk_bf16_f32 v144, v62, v4
	v_lshl_add_u64 v[160:161], v[52:53], 0, s[36:37]
	v_add_u32_e32 v4, s0, v60
	v_mov_b32_e32 v52, v3
	v_mov_b32_e32 v53, v3
	v_add_f32_e32 v153, 0, v5
	v_cvt_pk_bf16_f32 v145, v64, v8
	v_cvt_pk_bf16_f32 v146, v66, v12
	v_cvt_pk_bf16_f32 v147, v68, v16
	v_cvt_pk_bf16_f32 v140, v69, v20
	v_cvt_pk_bf16_f32 v141, v70, v24
	v_cvt_pk_bf16_f32 v142, v71, v28
	v_cvt_pk_bf16_f32 v143, v72, v32
	v_cvt_pk_bf16_f32 v132, v63, v6
	v_cvt_pk_bf16_f32 v133, v65, v10
	v_cvt_pk_bf16_f32 v134, v67, v14
	v_cvt_pk_bf16_f32 v135, v43, v18
	v_cvt_pk_bf16_f32 v136, v49, v22
	v_cvt_pk_bf16_f32 v137, v50, v26
	v_cvt_pk_bf16_f32 v138, v51, v30
	v_cvt_pk_bf16_f32 v139, v61, v34
	v_lshl_or_b32 v175, v39, 4, v42
	v_lshl_or_b32 v174, v44, 4, v41
	v_lshl_or_b32 v173, v45, 4, v42
	v_lshl_or_b32 v172, v46, 4, v41
	v_lshl_or_b32 v171, v47, 4, v42
	v_lshl_or_b32 v170, v48, 4, v41
	v_lshl_or_b32 v169, v40, 4, v42
	v_lshl_or_b32 v168, v38, 4, v41
	v_lshl_add_u64 v[154:155], v[58:59], 0, s[36:37]
	v_lshl_add_u64 v[156:157], v[54:55], 0, s[36:37]
	v_lshl_add_u64 v[158:159], v[56:57], 0, s[36:37]
	v_sub_u32_e32 v176, v4, v150
	v_mov_b32_e32 v54, v3
	v_mov_b32_e32 v55, v3
	v_mov_b32_e32 v56, v3
	v_mov_b32_e32 v57, v3
	v_mov_b32_e32 v58, v3
	v_mov_b32_e32 v59, v3
	v_mov_b32_e32 v60, v3
	v_mov_b32_e32 v61, v3
	v_mov_b32_e32 v62, v3
	v_mov_b32_e32 v63, v3
	v_mov_b32_e32 v64, v3
	v_mov_b32_e32 v65, v3
	v_mov_b32_e32 v66, v3
	v_mov_b32_e32 v67, v3
	v_mov_b64_e32 v[36:37], v[52:53]
	v_mov_b64_e32 v[20:21], v[52:53]
	v_mov_b64_e32 v[4:5], v[52:53]
	s_lshl_b32 s19, s19, 1
	s_or_b32 s24, s16, 31
	s_mov_b32 s25, 0x10000
	s_mov_b32 s31, 0x8000
	s_mov_b32 s0, 0
	s_movk_i32 s34, 0xffc0
	v_mov_b64_e32 v[38:39], v[54:55]
	v_mov_b64_e32 v[40:41], v[56:57]
	v_mov_b64_e32 v[42:43], v[58:59]
	v_mov_b64_e32 v[44:45], v[60:61]
	v_mov_b64_e32 v[46:47], v[62:63]
	v_mov_b64_e32 v[48:49], v[64:65]
	v_mov_b64_e32 v[50:51], v[66:67]
	v_mov_b64_e32 v[22:23], v[54:55]
	v_mov_b64_e32 v[24:25], v[56:57]
	v_mov_b64_e32 v[26:27], v[58:59]
	v_mov_b64_e32 v[28:29], v[60:61]
	v_mov_b64_e32 v[30:31], v[62:63]
	v_mov_b64_e32 v[32:33], v[64:65]
	v_mov_b64_e32 v[34:35], v[66:67]
	v_mov_b64_e32 v[6:7], v[54:55]
	v_mov_b64_e32 v[8:9], v[56:57]
	v_mov_b64_e32 v[10:11], v[58:59]
	v_mov_b64_e32 v[12:13], v[60:61]
	v_mov_b64_e32 v[14:15], v[62:63]
	v_mov_b64_e32 v[16:17], v[64:65]
	v_mov_b64_e32 v[18:19], v[66:67]
	s_mov_b32 s72, 0
	s_cmp_ge_u32 s72, s19
	s_mov_b32 s73, s0
	s_cselect_b32 s101, 0, 1
	s_branch .LBB0_397
.LBB0_395:
	s_mov_b32 s0, s31
	s_mov_b32 s31, s25
	s_mov_b32 s25, s73
	s_cmp_ge_u32 s72, s19
	s_mov_b32 s73, s0
	s_cselect_b32 s101, 0, 1
.LBB0_397:
	s_add_i32 s0, s34, 0x80
	s_cmp_le_u32 s0, s24
	s_cselect_b64 s[78:79], -1, 0
	s_add_i32 s82, s31, 0
	s_add_i32 s3, s34, 0x13f
	s_cmp_gt_u32 s3, s16
	s_cselect_b64 s[36:37], -1, 0
	s_cmp_gt_u32 s0, s24
	s_cbranch_scc1 .Latt_noqk
	v_add_u32_e32 v152, s82, v164
	ds_read_b128 v[204:207], v152
	ds_read_b128 v[208:211], v152 offset:512
	ds_read_b128 v[212:215], v152 offset:2048
	ds_read_b128 v[216:219], v152 offset:2560
	s_add_i32 s0, s73, 0
	v_add_u32_e32 v196, s0, v171
	v_add_u32_e32 v197, s0, v170
	v_add_u32_e32 v202, s0, v169
	v_add_u32_e32 v203, s0, v168
	ds_read_b64_tr_b16 v[178:179], v196 offset:16384
	ds_read_b64_tr_b16 v[180:181], v197 offset:16384
	ds_read_b64_tr_b16 v[184:185], v197 offset:20480
	ds_read_b64_tr_b16 v[182:183], v196 offset:20480
	ds_read_b64_tr_b16 v[186:187], v202 offset:16384
	ds_read_b64_tr_b16 v[188:189], v203 offset:16384
	ds_read_b64_tr_b16 v[192:193], v203 offset:20480
	ds_read_b64_tr_b16 v[190:191], v202 offset:20480
	v_cndmask_b32_e64 v68, v165, 0, s[36:37]
	v_sub_f32_e32 v68, v68, v167
	v_mov_b32_e32 v82, v68
	v_mov_b32_e32 v83, v68
	v_mov_b32_e32 v69, v68
	v_mov_b32_e32 v70, v68
	v_mov_b32_e32 v71, v68
	v_mov_b32_e32 v72, v68
	v_mov_b32_e32 v73, v68
	v_mov_b32_e32 v74, v68
	v_mov_b32_e32 v75, v68
	v_mov_b32_e32 v76, v68
	v_mov_b32_e32 v77, v68
	v_mov_b32_e32 v78, v68
	v_mov_b32_e32 v79, v68
	v_mov_b32_e32 v80, v68
	v_mov_b32_e32 v81, v68
	s_nop 1
	s_waitcnt lgkmcnt(11)
	v_mfma_f32_32x32x16_bf16 v[100:115], v[204:207], v[116:119], v[68:83]
	s_waitcnt lgkmcnt(10)
	v_mfma_f32_32x32x16_bf16 v[84:99], v[208:211], v[116:119], v[68:83]
	s_waitcnt lgkmcnt(9)
	v_mfma_f32_32x32x16_bf16 v[100:115], v[212:215], v[120:123], v[100:115]
	ds_read_b128 v[204:207], v152 offset:4096
	ds_read_b128 v[208:211], v152 offset:4608
	ds_read_b128 v[212:215], v152 offset:6144
	s_waitcnt lgkmcnt(11)
	v_mfma_f32_32x32x16_bf16 v[84:99], v[216:219], v[120:123], v[84:99]
	ds_read_b128 v[216:219], v152 offset:6656
	s_cmp_eq_u32 s101, 0
	s_cbranch_scc1 .Latt_dma_done
	s_add_i32 s0, s25, 0
	s_add_i32 s3, s0, s96
	s_mov_b32 s100, m0
	s_mov_b32 m0, s3
	s_nop 0
	global_load_lds_dwordx4 v[160:161], off
	s_mov_b32 m0, s100
	s_addk_i32 s3, 0x2000
	s_mov_b32 s100, m0
	s_mov_b32 m0, s3
	s_nop 0
	global_load_lds_dwordx4 v[158:159], off
	s_mov_b32 m0, s100
	s_add_i32 s0, s0, s97
	s_add_i32 s3, s0, 0x4000
	s_mov_b32 s100, m0
	s_mov_b32 m0, s3
	s_nop 0
	global_load_lds_dwordx4 v[156:157], off
	s_mov_b32 m0, s100
	s_addk_i32 s0, 0x4400
	s_mov_b32 s3, m0
	s_mov_b32 m0, s0
	s_nop 0
	global_load_lds_dwordx4 v[154:155], off
	s_mov_b32 m0, s3
.Latt_dma_done:
	s_waitcnt lgkmcnt(3)
	v_mfma_f32_32x32x16_bf16 v[100:115], v[204:207], v[124:127], v[100:115]
	s_waitcnt lgkmcnt(2)
	v_mfma_f32_32x32x16_bf16 v[84:99], v[208:211], v[124:127], v[84:99]
	s_waitcnt lgkmcnt(1)
	v_mfma_f32_32x32x16_bf16 v[68:83], v[212:215], v[128:131], v[100:115]
	s_waitcnt lgkmcnt(0)
	v_mfma_f32_32x32x16_bf16 v[84:99], v[216:219], v[128:131], v[84:99]
	s_andn2_b64 vcc, exec, s[36:37]
	s_cbranch_vccnz .LBB0_432
	v_add_u32_e32 v177, s5, v176
	s_mov_b32 s100, 0x207a4
	v_lshl_add_u32 v177, v177, 2, s100
	ds_read2_b32 v[204:205], v177 offset0:55 offset1:54
	ds_read2_b32 v[206:207], v177 offset0:53 offset1:52
	ds_read2_b32 v[208:209], v177 offset0:51 offset1:50
	ds_read2_b32 v[210:211], v177 offset0:49 offset1:48
	ds_read2_b32 v[212:213], v177 offset0:39 offset1:38
	ds_read2_b32 v[214:215], v177 offset0:37 offset1:36
	ds_read2_b32 v[216:217], v177 offset0:35 offset1:34
	ds_read2_b32 v[218:219], v177 offset0:33 offset1:32
	ds_read2_b32 v[220:221], v177 offset0:23 offset1:22
	ds_read2_b32 v[222:223], v177 offset0:21 offset1:20
	ds_read2_b32 v[224:225], v177 offset0:19 offset1:18
	ds_read2_b32 v[226:227], v177 offset0:17 offset1:16
	ds_read2_b32 v[228:229], v177 offset0:7 offset1:6
	ds_read2_b32 v[230:231], v177 offset0:5 offset1:4
	ds_read2_b32 v[232:233], v177 offset0:3 offset1:2
	s_waitcnt lgkmcnt(14)
	v_pk_add_f32 v[68:69], v[68:69], v[204:205]
	ds_read2_b32 v[204:205], v177 offset0:1 offset1:0
	s_waitcnt lgkmcnt(8)
	v_pk_add_f32 v[70:71], v[70:71], v[206:207]
	v_pk_add_f32 v[72:73], v[72:73], v[208:209]
	v_pk_add_f32 v[74:75], v[74:75], v[210:211]
	v_pk_add_f32 v[76:77], v[76:77], v[212:213]
	v_pk_add_f32 v[78:79], v[78:79], v[214:215]
	v_pk_add_f32 v[80:81], v[80:81], v[216:217]
	v_pk_add_f32 v[82:83], v[82:83], v[218:219]
	s_waitcnt lgkmcnt(0)
	v_pk_add_f32 v[84:85], v[84:85], v[220:221]
	v_pk_add_f32 v[86:87], v[86:87], v[222:223]
	v_pk_add_f32 v[88:89], v[88:89], v[224:225]
	v_pk_add_f32 v[90:91], v[90:91], v[226:227]
	v_pk_add_f32 v[92:93], v[92:93], v[228:229]
	v_pk_add_f32 v[94:95], v[94:95], v[230:231]
	v_pk_add_f32 v[96:97], v[96:97], v[232:233]
	v_pk_add_f32 v[98:99], v[98:99], v[204:205]

.Latt_noqk:
	s_cmp_eq_u32 s101, 0
	s_cbranch_scc1 .Latt_dma_done2
	s_add_i32 s0, s25, 0
	s_add_i32 s3, s0, s96
	s_mov_b32 s100, m0
	s_mov_b32 m0, s3
	s_nop 0
	global_load_lds_dwordx4 v[160:161], off
	s_mov_b32 m0, s100
	s_addk_i32 s3, 0x2000
	s_mov_b32 s100, m0
	s_mov_b32 m0, s3
	s_nop 0
	global_load_lds_dwordx4 v[158:159], off
	s_mov_b32 m0, s100
	s_add_i32 s0, s0, s97
	s_add_i32 s3, s0, 0x4000
	s_mov_b32 s100, m0
	s_mov_b32 m0, s3
	s_nop 0
	global_load_lds_dwordx4 v[156:157], off
	s_mov_b32 m0, s100
	s_addk_i32 s0, 0x4400
	s_mov_b32 s3, m0
	s_mov_b32 m0, s0
	s_nop 0
	global_load_lds_dwordx4 v[154:155], off
	s_mov_b32 m0, s3
